# K3 dsorted address generation on scalar unit with saddr loads; DPP pair swaps and immediate LDS offsets in final epilogue
# speedup vs baseline: 1.0261x; 1.0237x over previous
.LBB2_14:
	s_or_b64 exec, exec, s[2:3]
	s_and_saveexec_b64 s[2:3], s[4:5]
	s_movk_i32 s6, 0x30d4
	v_lshlrev_b32_e32 v5, 2, v102
	v_add_u32_e32 v7, 0x17850, v5
	v_add_u32_e32 v5, 0x17450, v5
	v_mad_u32_u24 v1, v102, s6, v2
	v_sub_u32_e32 v8, v3, v2
	ds_write_b32 v7, v1
	ds_write_b32 v5, v8
	s_or_b64 exec, exec, s[2:3]
	v_readfirstlane_b32 s86, v6
	v_lshlrev_b32_e32 v48, 4, v6
	v_lshlrev_b32_e32 v83, 2, v45
	s_mul_i32 s86, s86, 0xc3500
	s_add_u32 s86, s46, s86
	s_addc_u32 s87, s47, 0
	v_readlane_b32 s2, v2, 0
	v_readlane_b32 s3, v3, 0
	v_readlane_b32 s84, v2, 1
	v_readlane_b32 s85, v3, 1
	s_sub_i32 s42, s3, s2
	s_lshl_b32 s2, s2, 2
	s_add_u32 s88, s86, s2
	s_addc_u32 s89, s87, 0
	v_cmp_gt_u32_e64 s[20:21], s42, v45
	global_load_dword v18, v83, s[88:89]
	s_add_u32 s86, s86, 0xc350
	s_addc_u32 s87, s87, 0
	v_readlane_b32 s2, v2, 2
	v_readlane_b32 s3, v3, 2
	s_sub_i32 s50, s85, s84
	s_lshl_b32 s84, s84, 2
	s_add_u32 s90, s86, s84
	s_addc_u32 s91, s87, 0
	v_cmp_gt_u32_e64 s[8:9], s50, v45
	global_load_dword v16, v83, s[90:91]
	s_add_u32 s86, s86, 0xc350
	s_addc_u32 s87, s87, 0
	v_readlane_b32 s84, v2, 3
	v_readlane_b32 s85, v3, 3
	s_sub_i32 s48, s3, s2
	s_lshl_b32 s2, s2, 2
	s_add_u32 s92, s86, s2
	s_addc_u32 s93, s87, 0
	v_cmp_gt_u32_e64 s[10:11], s48, v45
	global_load_dword v14, v83, s[92:93]
	s_add_u32 s86, s86, 0xc350
	s_addc_u32 s87, s87, 0
	v_readlane_b32 s2, v2, 4
	v_readlane_b32 s3, v3, 4
	s_sub_i32 s43, s85, s84
	s_lshl_b32 s84, s84, 2
	s_add_u32 s94, s86, s84
	s_addc_u32 s95, s87, 0
	v_cmp_gt_u32_e64 s[12:13], s43, v45
	global_load_dword v13, v83, s[94:95]
	s_add_u32 s86, s86, 0xc350
	s_addc_u32 s87, s87, 0
	v_readlane_b32 s84, v2, 5
	v_readlane_b32 s85, v3, 5
	s_sub_i32 s51, s3, s2
	s_lshl_b32 s2, s2, 2
	s_add_u32 s88, s86, s2
	s_addc_u32 s89, s87, 0
	v_cmp_gt_u32_e64 s[14:15], s51, v45
	global_load_dword v11, v83, s[88:89]
	s_add_u32 s86, s86, 0xc350
	s_addc_u32 s87, s87, 0
	v_readlane_b32 s2, v2, 6
	v_readlane_b32 s3, v3, 6
	s_sub_i32 s49, s85, s84
	s_lshl_b32 s84, s84, 2
	s_add_u32 s90, s86, s84
	s_addc_u32 s91, s87, 0
	v_cmp_gt_u32_e64 s[16:17], s49, v45
	global_load_dword v9, v83, s[90:91]
	s_add_u32 s86, s86, 0xc350
	s_addc_u32 s87, s87, 0
	v_readlane_b32 s84, v2, 7
	v_readlane_b32 s85, v3, 7
	s_sub_i32 s66, s3, s2
	s_lshl_b32 s2, s2, 2
	s_add_u32 s92, s86, s2
	s_addc_u32 s93, s87, 0
	v_cmp_gt_u32_e64 s[18:19], s66, v45
	global_load_dword v8, v83, s[92:93]
	s_add_u32 s86, s86, 0xc350
	s_addc_u32 s87, s87, 0
	v_readlane_b32 s2, v2, 8
	v_readlane_b32 s3, v3, 8
	s_sub_i32 s65, s85, s84
	s_lshl_b32 s84, s84, 2
	s_add_u32 s94, s86, s84
	s_addc_u32 s95, s87, 0
	v_cmp_gt_u32_e64 s[22:23], s65, v45
	global_load_dword v7, v83, s[94:95]
	s_add_u32 s86, s86, 0xc350
	s_addc_u32 s87, s87, 0
	v_readlane_b32 s84, v2, 9
	v_readlane_b32 s85, v3, 9
	s_sub_i32 s68, s3, s2
	s_lshl_b32 s2, s2, 2
	s_add_u32 s88, s86, s2
	s_addc_u32 s89, s87, 0
	v_cmp_gt_u32_e64 s[24:25], s68, v45
	global_load_dword v17, v83, s[88:89]
	s_add_u32 s86, s86, 0xc350
	s_addc_u32 s87, s87, 0
	v_readlane_b32 s2, v2, 10
	v_readlane_b32 s3, v3, 10
	s_sub_i32 s67, s85, s84
	s_lshl_b32 s84, s84, 2
	s_add_u32 s90, s86, s84
	s_addc_u32 s91, s87, 0
	v_cmp_gt_u32_e64 s[26:27], s67, v45
	global_load_dword v15, v83, s[90:91]
	s_add_u32 s86, s86, 0xc350
	s_addc_u32 s87, s87, 0
	v_readlane_b32 s84, v2, 11
	v_readlane_b32 s85, v3, 11
	s_sub_i32 s70, s3, s2
	s_lshl_b32 s2, s2, 2
	s_add_u32 s92, s86, s2
	s_addc_u32 s93, s87, 0
	v_cmp_gt_u32_e64 s[28:29], s70, v45
	global_load_dword v12, v83, s[92:93]
	s_add_u32 s86, s86, 0xc350
	s_addc_u32 s87, s87, 0
	v_readlane_b32 s2, v2, 12
	v_readlane_b32 s3, v3, 12
	s_sub_i32 s69, s85, s84
	s_lshl_b32 s84, s84, 2
	s_add_u32 s94, s86, s84
	s_addc_u32 s95, s87, 0
	v_cmp_gt_u32_e64 s[30:31], s69, v45
	global_load_dword v10, v83, s[94:95]
	s_add_u32 s86, s86, 0xc350
	s_addc_u32 s87, s87, 0
	v_readlane_b32 s84, v2, 13
	v_readlane_b32 s85, v3, 13
	s_sub_i32 s72, s3, s2
	s_lshl_b32 s2, s2, 2
	s_add_u32 s88, s86, s2
	s_addc_u32 s89, s87, 0
	v_cmp_gt_u32_e64 s[34:35], s72, v45
	global_load_dword v5, v83, s[88:89]
	s_add_u32 s86, s86, 0xc350
	s_addc_u32 s87, s87, 0
	v_readlane_b32 s2, v2, 14
	v_readlane_b32 s3, v3, 14
	s_sub_i32 s71, s85, s84
	s_lshl_b32 s84, s84, 2
	s_add_u32 s90, s86, s84
	s_addc_u32 s91, s87, 0
	v_cmp_gt_u32_e64 s[36:37], s71, v45
	global_load_dword v4, v83, s[90:91]
	s_add_u32 s86, s86, 0xc350
	s_addc_u32 s87, s87, 0
	v_readlane_b32 s84, v2, 15
	v_readlane_b32 s85, v3, 15
	s_sub_i32 s74, s3, s2
	s_lshl_b32 s2, s2, 2
	s_add_u32 s92, s86, s2
	s_addc_u32 s93, s87, 0
	v_cmp_gt_u32_e64 s[6:7], s74, v45
	global_load_dword v3, v83, s[92:93]
	s_add_u32 s86, s86, 0xc350
	s_addc_u32 s87, s87, 0
	s_sub_i32 s73, s85, s84
	s_lshl_b32 s84, s84, 2
	s_add_u32 s94, s86, s84
	s_addc_u32 s95, s87, 0
	v_cmp_gt_u32_e32 vcc, s73, v45
	global_load_dword v2, v83, s[94:95]
	s_barrier
	s_getreg_b32 s2, hwreg(HW_REG_XCC_ID, 0, 4)
	s_and_b32 s33, s2, 15
	s_and_saveexec_b64 s[38:39], s[44:45]
	s_cbranch_execz .LBB2_17
	s_mov_b64 s[40:41], exec
	v_mbcnt_lo_u32_b32 v19, s40, 0
	v_mbcnt_hi_u32_b32 v19, s41, v19
	v_cmp_eq_u32_e64 s[2:3], 0, v19
	s_and_b64 s[2:3], exec, s[2:3]
	s_mov_b64 exec, s[2:3]
	s_cbranch_execz .LBB2_17
	s_lshl_b32 s2, s33, 8
	s_bcnt1_i32_b64 s3, s[40:41]
	v_mov_b32_e32 v19, s2
	v_mov_b32_e32 v20, s3
	global_atomic_add v19, v20, s[54:55] offset:1024

.LBB2_369:
	v_xor_b32_e32 v0, 1, v51
	v_add_u32_e32 v1, 64, v52
	v_cmp_lt_i32_e32 vcc, v0, v1
	s_waitcnt lgkmcnt(0)
	v_mul_f32_e32 v2, v53, v2
	v_cndmask_b32_e32 v0, v51, v0, vcc
	v_lshlrev_b32_e32 v65, 2, v0
	v_mul_f32_e32 v0, v53, v6
	s_nop 1
	v_mov_b32_dpp v1, v0 quad_perm:[1,0,3,2] row_mask:0xf bank_mask:0xf
	v_cmp_eq_u32_e32 vcc, 0, v44
	v_mul_f32_e32 v6, v53, v7
	s_nop 1
	v_mov_b32_dpp v7, v6 quad_perm:[1,0,3,2] row_mask:0xf bank_mask:0xf
	s_waitcnt lgkmcnt(1)
	v_cndmask_b32_e32 v52, v1, v0, vcc
	v_cndmask_b32_e32 v70, v0, v1, vcc
	v_mul_f32_e32 v0, v53, v8
	s_nop 1
	v_mov_b32_dpp v1, v0 quad_perm:[1,0,3,2] row_mask:0xf bank_mask:0xf
	s_nop 1
	v_mov_b32_dpp v8, v2 quad_perm:[1,0,3,2] row_mask:0xf bank_mask:0xf
	s_waitcnt lgkmcnt(2)
	v_cndmask_b32_e32 v54, v7, v6, vcc
	v_cndmask_b32_e32 v68, v6, v7, vcc
	v_mul_f32_e32 v6, v53, v9
	s_waitcnt lgkmcnt(1)
	v_cndmask_b32_e32 v56, v1, v0, vcc
	v_cndmask_b32_e32 v76, v0, v1, vcc
	v_mul_f32_e32 v0, v53, v3
	s_nop 1
	v_mov_b32_dpp v1, v0 quad_perm:[1,0,3,2] row_mask:0xf bank_mask:0xf
	s_waitcnt lgkmcnt(1)
	v_cndmask_b32_e32 v60, v8, v2, vcc
	v_cndmask_b32_e32 v72, v2, v8, vcc
	v_mul_f32_e32 v2, v53, v4
	v_mul_f32_e32 v4, v53, v5
	s_nop 1
	v_mov_b32_dpp v5, v4 quad_perm:[1,0,3,2] row_mask:0xf bank_mask:0xf
	s_nop 1
	v_mov_b32_dpp v3, v2 quad_perm:[1,0,3,2] row_mask:0xf bank_mask:0xf
	s_nop 1
	v_mov_b32_dpp v7, v6 quad_perm:[1,0,3,2] row_mask:0xf bank_mask:0xf
	s_waitcnt lgkmcnt(3)
	v_cndmask_b32_e32 v62, v1, v0, vcc
	v_cndmask_b32_e32 v82, v0, v1, vcc
	v_mul_u32_u24_e32 v0, 20, v44
	v_lshlrev_b32_e32 v66, 2, v0
	s_waitcnt lgkmcnt(2)
	v_cndmask_b32_e32 v84, v5, v4, vcc
	v_cndmask_b32_e32 v78, v4, v5, vcc
	v_add_u32_e32 v66, 0x16400, v66
	s_waitcnt lgkmcnt(1)
	v_cndmask_b32_e32 v86, v3, v2, vcc
	v_cndmask_b32_e32 v80, v2, v3, vcc
	ds_read_b128 v[48:51], v66 offset:6224
	ds_read_b128 v[88:91], v66 offset:6240
	ds_read_b128 v[32:35], v66 offset:6256
	ds_read_b128 v[16:19], v66 offset:6272
	ds_read_b128 v[0:3], v66 offset:6288
	ds_read_b128 v[92:95], v66
	ds_read_b128 v[96:99], v66 offset:16
	ds_read_b128 v[40:43], v66 offset:32
	s_waitcnt lgkmcnt(8)
	v_cndmask_b32_e32 v58, v7, v6, vcc
	v_cndmask_b32_e32 v74, v6, v7, vcc
	ds_read_b128 v[20:23], v66 offset:48
	ds_read_b128 v[4:7], v66 offset:64
	ds_read_b128 v[100:103], v66 offset:160
	ds_read_b128 v[104:107], v66 offset:176
	ds_read_b128 v[36:39], v66 offset:192
	ds_read_b128 v[24:27], v66 offset:208
	s_waitcnt vmcnt(0)
	ds_read_b128 v[8:11], v66 offset:224
	ds_read_b128 v[108:111], v66 offset:320
	ds_read_b128 v[112:115], v66 offset:336
	ds_read_b128 v[44:47], v66 offset:352
	ds_read_b128 v[28:31], v66 offset:368
	ds_read_b128 v[12:15], v66 offset:384
	s_waitcnt lgkmcnt(14)
	v_pk_fma_f32 v[48:49], v[52:53], v[92:93], v[48:49] op_sel_hi:[0,1,1]
	v_pk_fma_f32 v[50:51], v[52:53], v[94:95], v[50:51] op_sel_hi:[0,1,1]
	ds_read_b128 v[92:95], v66 offset:480
	ds_read_b128 v[116:119], v66 offset:496
	s_waitcnt lgkmcnt(11)
	v_pk_fma_f32 v[48:49], v[54:55], v[100:101], v[48:49] op_sel_hi:[0,1,1]
	v_pk_fma_f32 v[50:51], v[54:55], v[102:103], v[50:51] op_sel_hi:[0,1,1]
	ds_read_b128 v[120:123], v66 offset:512
	ds_read_b128 v[124:127], v66 offset:528
	s_waitcnt lgkmcnt(8)
	v_pk_fma_f32 v[100:101], v[56:57], v[108:109], v[48:49] op_sel_hi:[0,1,1]
	v_pk_fma_f32 v[102:103], v[56:57], v[110:111], v[50:51] op_sel_hi:[0,1,1]
	v_pk_fma_f32 v[96:97], v[52:53], v[96:97], v[88:89] op_sel_hi:[0,1,1]
	v_pk_fma_f32 v[108:109], v[52:53], v[98:99], v[90:91] op_sel_hi:[0,1,1]
	ds_read_b128 v[48:51], v66 offset:544
	ds_read_b128 v[88:91], v66 offset:640
	s_waitcnt lgkmcnt(5)
	v_pk_fma_f32 v[98:99], v[58:59], v[92:93], v[100:101] op_sel_hi:[0,1,1]
	v_pk_fma_f32 v[100:101], v[58:59], v[94:95], v[102:103] op_sel_hi:[0,1,1]
	ds_read_b128 v[92:95], v66 offset:800
	s_waitcnt lgkmcnt(1)
	v_pk_fma_f32 v[98:99], v[60:61], v[88:89], v[98:99] op_sel_hi:[0,1,1]
	v_pk_fma_f32 v[100:101], v[60:61], v[90:91], v[100:101] op_sel_hi:[0,1,1]
	ds_read_b128 v[88:91], v66 offset:816
	s_waitcnt lgkmcnt(1)
	v_pk_fma_f32 v[98:99], v[62:63], v[92:93], v[98:99] op_sel_hi:[0,1,1]
	v_pk_fma_f32 v[92:93], v[62:63], v[94:95], v[100:101] op_sel_hi:[0,1,1]
	v_pk_fma_f32 v[100:101], v[54:55], v[104:105], v[96:97] op_sel_hi:[0,1,1]
	v_pk_fma_f32 v[102:103], v[54:55], v[106:107], v[108:109] op_sel_hi:[0,1,1]
	ds_read_b128 v[94:97], v66 offset:656
	ds_read_b128 v[108:111], v66 offset:672
	v_pk_fma_f32 v[100:101], v[56:57], v[112:113], v[100:101] op_sel_hi:[0,1,1]
	v_pk_fma_f32 v[102:103], v[56:57], v[114:115], v[102:103] op_sel_hi:[0,1,1]
	v_pk_fma_f32 v[100:101], v[58:59], v[116:117], v[100:101] op_sel_hi:[0,1,1]
	v_pk_fma_f32 v[102:103], v[58:59], v[118:119], v[102:103] op_sel_hi:[0,1,1]
	ds_read_b128 v[112:115], v66 offset:688
	ds_read_b128 v[116:119], v66 offset:704
	v_pk_fma_f32 v[32:33], v[52:53], v[40:41], v[32:33] op_sel_hi:[0,1,1]
	v_pk_fma_f32 v[32:33], v[54:55], v[36:37], v[32:33] op_sel_hi:[0,1,1]
	v_pk_fma_f32 v[32:33], v[56:57], v[44:45], v[32:33] op_sel_hi:[0,1,1]
	s_waitcnt lgkmcnt(3)
	v_pk_fma_f32 v[94:95], v[60:61], v[94:95], v[100:101] op_sel_hi:[0,1,1]
	v_pk_fma_f32 v[32:33], v[58:59], v[120:121], v[32:33] op_sel_hi:[0,1,1]
	v_pk_fma_f32 v[106:107], v[62:63], v[88:89], v[94:95] op_sel_hi:[0,1,1]
	v_pk_fma_f32 v[88:89], v[60:61], v[96:97], v[102:103] op_sel_hi:[0,1,1]
	s_waitcnt lgkmcnt(2)
	v_pk_fma_f32 v[36:37], v[60:61], v[108:109], v[32:33] op_sel_hi:[0,1,1]
	v_pk_fma_f32 v[104:105], v[62:63], v[90:91], v[88:89] op_sel_hi:[0,1,1]
	ds_read_b128 v[88:91], v66 offset:832
	v_pk_fma_f32 v[40:41], v[52:53], v[42:43], v[34:35] op_sel_hi:[0,1,1]
	ds_read_b128 v[32:35], v66 offset:848
	v_pk_fma_f32 v[16:17], v[52:53], v[20:21], v[16:17] op_sel_hi:[0,1,1]
	v_pk_fma_f32 v[16:17], v[54:55], v[24:25], v[16:17] op_sel_hi:[0,1,1]
	v_pk_fma_f32 v[16:17], v[56:57], v[28:29], v[16:17] op_sel_hi:[0,1,1]
	v_pk_fma_f32 v[16:17], v[58:59], v[124:125], v[16:17] op_sel_hi:[0,1,1]
	s_waitcnt lgkmcnt(3)
	v_pk_fma_f32 v[16:17], v[60:61], v[112:113], v[16:17] op_sel_hi:[0,1,1]
	s_waitcnt lgkmcnt(1)
	v_pk_fma_f32 v[102:103], v[62:63], v[88:89], v[36:37] op_sel_hi:[0,1,1]
	s_waitcnt lgkmcnt(0)
	v_pk_fma_f32 v[88:89], v[62:63], v[32:33], v[16:17] op_sel_hi:[0,1,1]
	v_pk_fma_f32 v[16:17], v[52:53], v[22:23], v[18:19] op_sel_hi:[0,1,1]
	v_pk_fma_f32 v[16:17], v[54:55], v[26:27], v[16:17] op_sel_hi:[0,1,1]
	v_pk_fma_f32 v[16:17], v[56:57], v[30:31], v[16:17] op_sel_hi:[0,1,1]
	v_pk_fma_f32 v[16:17], v[58:59], v[126:127], v[16:17] op_sel_hi:[0,1,1]
	v_pk_fma_f32 v[16:17], v[60:61], v[114:115], v[16:17] op_sel_hi:[0,1,1]
	v_pk_fma_f32 v[94:95], v[62:63], v[34:35], v[16:17] op_sel_hi:[0,1,1]
	ds_read_b128 v[16:19], v66 offset:864
	v_pk_fma_f32 v[0:1], v[52:53], v[4:5], v[0:1] op_sel_hi:[0,1,1]
	v_pk_fma_f32 v[0:1], v[54:55], v[8:9], v[0:1] op_sel_hi:[0,1,1]
	v_pk_fma_f32 v[0:1], v[56:57], v[12:13], v[0:1] op_sel_hi:[0,1,1]
	v_pk_fma_f32 v[0:1], v[58:59], v[48:49], v[0:1] op_sel_hi:[0,1,1]
	v_pk_fma_f32 v[0:1], v[60:61], v[116:117], v[0:1] op_sel_hi:[0,1,1]
	ds_read_b128 v[32:35], v66 offset:960
	s_waitcnt lgkmcnt(1)
	v_pk_fma_f32 v[96:97], v[62:63], v[16:17], v[0:1] op_sel_hi:[0,1,1]
	v_pk_fma_f32 v[0:1], v[52:53], v[6:7], v[2:3] op_sel_hi:[0,1,1]
	v_pk_fma_f32 v[36:37], v[54:55], v[38:39], v[40:41] op_sel_hi:[0,1,1]
	v_pk_fma_f32 v[0:1], v[54:55], v[10:11], v[0:1] op_sel_hi:[0,1,1]
	v_pk_fma_f32 v[36:37], v[56:57], v[46:47], v[36:37] op_sel_hi:[0,1,1]
	v_pk_fma_f32 v[0:1], v[56:57], v[14:15], v[0:1] op_sel_hi:[0,1,1]
	v_pk_fma_f32 v[36:37], v[58:59], v[122:123], v[36:37] op_sel_hi:[0,1,1]
	v_pk_fma_f32 v[0:1], v[58:59], v[50:51], v[0:1] op_sel_hi:[0,1,1]
	v_pk_fma_f32 v[36:37], v[60:61], v[110:111], v[36:37] op_sel_hi:[0,1,1]
	v_pk_fma_f32 v[0:1], v[60:61], v[118:119], v[0:1] op_sel_hi:[0,1,1]
	v_pk_fma_f32 v[100:101], v[62:63], v[90:91], v[36:37] op_sel_hi:[0,1,1]
	v_pk_fma_f32 v[90:91], v[62:63], v[18:19], v[0:1] op_sel_hi:[0,1,1]
	ds_read_b128 v[48:51], v66 offset:976
	ds_read_b128 v[28:31], v66 offset:992
	ds_read_b128 v[16:19], v66 offset:1008
	ds_read_b128 v[0:3], v66 offset:1024
	ds_read_b128 v[44:47], v66 offset:1120
	ds_read_b128 v[52:55], v66 offset:1136
	ds_read_b128 v[36:39], v66 offset:1152
	ds_read_b128 v[20:23], v66 offset:1168
	ds_read_b128 v[4:7], v66 offset:1184
	ds_read_b128 v[108:111], v66 offset:1280
	ds_read_b128 v[56:59], v66 offset:1296
	ds_read_b128 v[40:43], v66 offset:1312
	ds_read_b128 v[24:27], v66 offset:1328
	ds_read_b128 v[8:11], v66 offset:1344
	ds_read_b128 v[112:115], v66 offset:1440
	ds_read_b128 v[60:63], v66 offset:1456
	ds_read_b128 v[12:15], v66 offset:1504
	ds_read_b128 v[116:119], v66 offset:1600
	s_waitcnt lgkmcnt(14)
	v_pk_fma_f32 v[32:33], v[86:87], v[32:33], v[98:99] op_sel_hi:[0,1,1]
	v_pk_fma_f32 v[34:35], v[86:87], v[34:35], v[92:93] op_sel_hi:[0,1,1]
	s_waitcnt lgkmcnt(13)
	v_pk_fma_f32 v[32:33], v[84:85], v[44:45], v[32:33] op_sel_hi:[0,1,1]
	v_pk_fma_f32 v[34:35], v[84:85], v[46:47], v[34:35] op_sel_hi:[0,1,1]
	ds_read_b128 v[120:123], v66 offset:1760
	ds_read_b128 v[124:127], v66 offset:1776
	s_waitcnt lgkmcnt(10)
	v_pk_fma_f32 v[92:93], v[70:71], v[108:109], v[32:33] op_sel_hi:[0,1,1]
	v_pk_fma_f32 v[98:99], v[70:71], v[110:111], v[34:35] op_sel_hi:[0,1,1]
	ds_read_b128 v[32:35], v66 offset:1824
	ds_read_b128 v[44:47], v66 offset:1920
	s_waitcnt lgkmcnt(7)
	v_pk_fma_f32 v[92:93], v[68:69], v[112:113], v[92:93] op_sel_hi:[0,1,1]
	v_pk_fma_f32 v[98:99], v[68:69], v[114:115], v[98:99] op_sel_hi:[0,1,1]
	ds_read_b128 v[108:111], v66 offset:2080
	ds_read_b128 v[112:115], v66 offset:2096
	s_waitcnt lgkmcnt(6)
	v_pk_fma_f32 v[92:93], v[76:77], v[116:117], v[92:93] op_sel_hi:[0,1,1]
	v_pk_fma_f32 v[98:99], v[76:77], v[118:119], v[98:99] op_sel_hi:[0,1,1]
	s_waitcnt lgkmcnt(5)
	v_pk_fma_f32 v[92:93], v[74:75], v[120:121], v[92:93] op_sel_hi:[0,1,1]
	v_pk_fma_f32 v[98:99], v[74:75], v[122:123], v[98:99] op_sel_hi:[0,1,1]
	s_waitcnt lgkmcnt(2)
	v_pk_fma_f32 v[92:93], v[72:73], v[44:45], v[92:93] op_sel_hi:[0,1,1]
	v_pk_fma_f32 v[98:99], v[72:73], v[46:47], v[98:99] op_sel_hi:[0,1,1]
	ds_read_b128 v[44:47], v66 offset:2144
	ds_read_b128 v[116:119], v66 offset:2240
	s_waitcnt lgkmcnt(3)
	v_pk_fma_f32 v[92:93], v[82:83], v[108:109], v[92:93] op_sel_hi:[0,1,1]
	v_pk_fma_f32 v[98:99], v[82:83], v[110:111], v[98:99] op_sel_hi:[0,1,1]
	ds_read_b128 v[108:111], v66 offset:2400
	s_waitcnt lgkmcnt(1)
	v_pk_fma_f32 v[92:93], v[80:81], v[116:117], v[92:93] op_sel_hi:[0,1,1]
	v_pk_fma_f32 v[98:99], v[80:81], v[118:119], v[98:99] op_sel_hi:[0,1,1]
	s_waitcnt lgkmcnt(0)
	v_pk_fma_f32 v[92:93], v[78:79], v[108:109], v[92:93] op_sel_hi:[0,1,1]
	v_pk_fma_f32 v[98:99], v[78:79], v[110:111], v[98:99] op_sel_hi:[0,1,1]
	v_pk_fma_f32 v[108:109], v[86:87], v[48:49], v[106:107] op_sel_hi:[0,1,1]
	v_pk_fma_f32 v[110:111], v[86:87], v[50:51], v[104:105] op_sel_hi:[0,1,1]
	ds_read_b128 v[116:119], v66 offset:2416
	ds_read_b128 v[104:107], v66 offset:1472
	ds_read_b128 v[48:51], v66 offset:1488
	v_pk_fma_f32 v[52:53], v[84:85], v[52:53], v[108:109] op_sel_hi:[0,1,1]
	v_pk_fma_f32 v[54:55], v[84:85], v[54:55], v[110:111] op_sel_hi:[0,1,1]
	v_pk_fma_f32 v[56:57], v[70:71], v[56:57], v[52:53] op_sel_hi:[0,1,1]
	v_pk_fma_f32 v[58:59], v[70:71], v[58:59], v[54:55] op_sel_hi:[0,1,1]
	ds_read_b128 v[52:55], v66 offset:1616
	ds_read_b128 v[108:111], v66 offset:1632
	v_pk_fma_f32 v[56:57], v[68:69], v[60:61], v[56:57] op_sel_hi:[0,1,1]
	v_pk_fma_f32 v[58:59], v[68:69], v[62:63], v[58:59] op_sel_hi:[0,1,1]
	s_waitcnt lgkmcnt(1)
	v_pk_fma_f32 v[56:57], v[76:77], v[52:53], v[56:57] op_sel_hi:[0,1,1]
	v_pk_fma_f32 v[58:59], v[76:77], v[54:55], v[58:59] op_sel_hi:[0,1,1]
	ds_read_b128 v[52:55], v66 offset:1936
	v_pk_fma_f32 v[56:57], v[74:75], v[124:125], v[56:57] op_sel_hi:[0,1,1]
	v_pk_fma_f32 v[58:59], v[74:75], v[126:127], v[58:59] op_sel_hi:[0,1,1]
	ds_read_b128 v[60:63], v66 offset:1952
	s_waitcnt lgkmcnt(1)
	v_pk_fma_f32 v[56:57], v[72:73], v[52:53], v[56:57] op_sel_hi:[0,1,1]
	v_pk_fma_f32 v[58:59], v[72:73], v[54:55], v[58:59] op_sel_hi:[0,1,1]
	ds_read_b128 v[52:55], v66 offset:2256
	v_pk_fma_f32 v[56:57], v[82:83], v[112:113], v[56:57] op_sel_hi:[0,1,1]
	v_pk_fma_f32 v[58:59], v[82:83], v[114:115], v[58:59] op_sel_hi:[0,1,1]
	s_waitcnt lgkmcnt(0)
	v_pk_fma_f32 v[56:57], v[80:81], v[52:53], v[56:57] op_sel_hi:[0,1,1]
	v_pk_fma_f32 v[58:59], v[80:81], v[54:55], v[58:59] op_sel_hi:[0,1,1]
	v_pk_fma_f32 v[56:57], v[78:79], v[116:117], v[56:57] op_sel_hi:[0,1,1]
	v_pk_fma_f32 v[58:59], v[78:79], v[118:119], v[58:59] op_sel_hi:[0,1,1]
	v_pk_fma_f32 v[116:117], v[86:87], v[28:29], v[102:103] op_sel_hi:[0,1,1]
	v_pk_fma_f32 v[118:119], v[86:87], v[30:31], v[100:101] op_sel_hi:[0,1,1]
	ds_read_b128 v[112:115], v66 offset:2272
	ds_read_b128 v[120:123], v66 offset:1648
	ds_read_b128 v[52:55], v66 offset:1664
	v_pk_fma_f32 v[36:37], v[84:85], v[36:37], v[116:117] op_sel_hi:[0,1,1]
	v_pk_fma_f32 v[38:39], v[84:85], v[38:39], v[118:119] op_sel_hi:[0,1,1]
	ds_read_b128 v[28:31], v66 offset:1792
	ds_read_b128 v[100:103], v66 offset:1808
	v_pk_fma_f32 v[116:117], v[70:71], v[40:41], v[36:37] op_sel_hi:[0,1,1]
	v_pk_fma_f32 v[118:119], v[70:71], v[42:43], v[38:39] op_sel_hi:[0,1,1]
	ds_read_b128 v[36:39], v66 offset:1968
	ds_read_b128 v[40:43], v66 offset:1984
	v_pk_fma_f32 v[104:105], v[68:69], v[104:105], v[116:117] op_sel_hi:[0,1,1]
	v_pk_fma_f32 v[106:107], v[68:69], v[106:107], v[118:119] op_sel_hi:[0,1,1]
	v_pk_fma_f32 v[116:117], v[76:77], v[108:109], v[104:105] op_sel_hi:[0,1,1]
	v_pk_fma_f32 v[118:119], v[76:77], v[110:111], v[106:107] op_sel_hi:[0,1,1]
	ds_read_b128 v[104:107], v66 offset:2112
	ds_read_b128 v[108:111], v66 offset:2128
	s_waitcnt lgkmcnt(5)
	v_pk_fma_f32 v[28:29], v[74:75], v[28:29], v[116:117] op_sel_hi:[0,1,1]
	v_pk_fma_f32 v[30:31], v[74:75], v[30:31], v[118:119] op_sel_hi:[0,1,1]
	v_pk_fma_f32 v[16:17], v[86:87], v[16:17], v[88:89] op_sel_hi:[0,1,1]
	v_pk_fma_f32 v[28:29], v[72:73], v[60:61], v[28:29] op_sel_hi:[0,1,1]
	v_pk_fma_f32 v[30:31], v[72:73], v[62:63], v[30:31] op_sel_hi:[0,1,1]
	ds_read_b128 v[60:63], v66 offset:2288
	ds_read_b128 v[116:119], v66 offset:2304
	v_pk_fma_f32 v[16:17], v[84:85], v[20:21], v[16:17] op_sel_hi:[0,1,1]
	v_pk_fma_f32 v[18:19], v[86:87], v[18:19], v[94:95] op_sel_hi:[0,1,1]
	s_waitcnt lgkmcnt(3)
	v_pk_fma_f32 v[104:105], v[82:83], v[104:105], v[28:29] op_sel_hi:[0,1,1]
	v_pk_fma_f32 v[106:107], v[82:83], v[106:107], v[30:31] op_sel_hi:[0,1,1]
	ds_read_b128 v[28:31], v66 offset:2432
	v_pk_fma_f32 v[16:17], v[70:71], v[24:25], v[16:17] op_sel_hi:[0,1,1]
	v_pk_fma_f32 v[18:19], v[84:85], v[22:23], v[18:19] op_sel_hi:[0,1,1]
	v_pk_fma_f32 v[0:1], v[86:87], v[0:1], v[96:97] op_sel_hi:[0,1,1]
	v_pk_fma_f32 v[16:17], v[68:69], v[48:49], v[16:17] op_sel_hi:[0,1,1]
	v_pk_fma_f32 v[18:19], v[70:71], v[26:27], v[18:19] op_sel_hi:[0,1,1]
	ds_read_b128 v[20:23], v66 offset:2464
	v_pk_fma_f32 v[0:1], v[84:85], v[4:5], v[0:1] op_sel_hi:[0,1,1]
	v_pk_fma_f32 v[2:3], v[86:87], v[2:3], v[90:91] op_sel_hi:[0,1,1]
	v_pk_fma_f32 v[112:113], v[80:81], v[112:113], v[104:105] op_sel_hi:[0,1,1]
	v_pk_fma_f32 v[114:115], v[80:81], v[114:115], v[106:107] op_sel_hi:[0,1,1]
	ds_read_b128 v[104:107], v66 offset:2448
	v_subrev_u32_e32 v66, 0x16400, v66
	v_pk_fma_f32 v[16:17], v[76:77], v[120:121], v[16:17] op_sel_hi:[0,1,1]
	v_pk_fma_f32 v[18:19], v[68:69], v[50:51], v[18:19] op_sel_hi:[0,1,1]
	v_pk_fma_f32 v[0:1], v[70:71], v[8:9], v[0:1] op_sel_hi:[0,1,1]
	v_pk_fma_f32 v[2:3], v[84:85], v[6:7], v[2:3] op_sel_hi:[0,1,1]
	v_max_f32_e32 v4, v92, v93
	v_pk_fma_f32 v[16:17], v[74:75], v[100:101], v[16:17] op_sel_hi:[0,1,1]
	v_pk_fma_f32 v[18:19], v[76:77], v[122:123], v[18:19] op_sel_hi:[0,1,1]
	v_pk_fma_f32 v[0:1], v[68:69], v[12:13], v[0:1] op_sel_hi:[0,1,1]
	v_pk_fma_f32 v[2:3], v[70:71], v[10:11], v[2:3] op_sel_hi:[0,1,1]
	v_max3_f32 v4, v4, v98, v99
	v_pk_fma_f32 v[16:17], v[72:73], v[36:37], v[16:17] op_sel_hi:[0,1,1]
	v_pk_fma_f32 v[18:19], v[74:75], v[102:103], v[18:19] op_sel_hi:[0,1,1]
	v_pk_fma_f32 v[0:1], v[76:77], v[52:53], v[0:1] op_sel_hi:[0,1,1]
	v_pk_fma_f32 v[2:3], v[68:69], v[14:15], v[2:3] op_sel_hi:[0,1,1]
	v_max3_f32 v4, v4, v56, v57
	s_waitcnt lgkmcnt(2)
	v_pk_fma_f32 v[28:29], v[78:79], v[28:29], v[112:113] op_sel_hi:[0,1,1]
	v_pk_fma_f32 v[16:17], v[82:83], v[108:109], v[16:17] op_sel_hi:[0,1,1]
	v_pk_fma_f32 v[18:19], v[72:73], v[38:39], v[18:19] op_sel_hi:[0,1,1]
	v_pk_fma_f32 v[0:1], v[74:75], v[32:33], v[0:1] op_sel_hi:[0,1,1]
	v_pk_fma_f32 v[2:3], v[76:77], v[54:55], v[2:3] op_sel_hi:[0,1,1]
	v_max3_f32 v4, v4, v58, v59
	v_pk_fma_f32 v[30:31], v[78:79], v[30:31], v[114:115] op_sel_hi:[0,1,1]
	v_pk_fma_f32 v[16:17], v[80:81], v[60:61], v[16:17] op_sel_hi:[0,1,1]
	v_pk_fma_f32 v[18:19], v[82:83], v[110:111], v[18:19] op_sel_hi:[0,1,1]
	v_pk_fma_f32 v[0:1], v[72:73], v[40:41], v[0:1] op_sel_hi:[0,1,1]
	v_pk_fma_f32 v[2:3], v[74:75], v[34:35], v[2:3] op_sel_hi:[0,1,1]
	v_max3_f32 v4, v4, v28, v29
	s_waitcnt lgkmcnt(0)
	v_pk_fma_f32 v[16:17], v[78:79], v[104:105], v[16:17] op_sel_hi:[0,1,1]
	v_pk_fma_f32 v[18:19], v[80:81], v[62:63], v[18:19] op_sel_hi:[0,1,1]
	v_pk_fma_f32 v[0:1], v[82:83], v[44:45], v[0:1] op_sel_hi:[0,1,1]
	v_pk_fma_f32 v[2:3], v[72:73], v[42:43], v[2:3] op_sel_hi:[0,1,1]
	v_max3_f32 v4, v4, v30, v31
	v_pk_fma_f32 v[18:19], v[78:79], v[106:107], v[18:19] op_sel_hi:[0,1,1]
	v_pk_fma_f32 v[0:1], v[80:81], v[116:117], v[0:1] op_sel_hi:[0,1,1]
	v_pk_fma_f32 v[2:3], v[82:83], v[46:47], v[2:3] op_sel_hi:[0,1,1]
	v_max3_f32 v4, v4, v16, v17
	v_pk_fma_f32 v[0:1], v[78:79], v[20:21], v[0:1] op_sel_hi:[0,1,1]
	v_pk_fma_f32 v[2:3], v[80:81], v[118:119], v[2:3] op_sel_hi:[0,1,1]
	v_max3_f32 v4, v4, v18, v19
	v_pk_fma_f32 v[2:3], v[78:79], v[22:23], v[2:3] op_sel_hi:[0,1,1]
	v_max3_f32 v4, v4, v0, v1
	v_max3_f32 v4, v4, v2, v3
	s_nop 1
	v_mov_b32_dpp v5, v4 quad_perm:[1,0,3,2] row_mask:0xf bank_mask:0xf
	s_waitcnt lgkmcnt(0)
	v_max_f32_e32 v5, v5, v5
	v_max_f32_e32 v4, v4, v5
	v_sub_f32_e32 v5, v92, v4
	v_mul_f32_e32 v5, 0x3fb8aa3b, v5
	v_sub_f32_e32 v6, v93, v4
	v_exp_f32_e32 v5, v5
	v_mul_f32_e32 v6, 0x3fb8aa3b, v6
	v_sub_f32_e32 v7, v98, v4
	v_exp_f32_e32 v6, v6
	v_mul_f32_e32 v7, 0x3fb8aa3b, v7
	v_sub_f32_e32 v8, v99, v4
	v_exp_f32_e32 v7, v7
	v_mul_f32_e32 v8, 0x3fb8aa3b, v8
	v_exp_f32_e32 v8, v8
	v_add_f32_e32 v5, 0, v5
	v_add_f32_e32 v5, v5, v6
	v_sub_f32_e32 v6, v56, v4
	v_add_f32_e32 v5, v5, v7
	v_mul_f32_e32 v6, 0x3fb8aa3b, v6
	v_sub_f32_e32 v7, v57, v4
	v_add_f32_e32 v5, v5, v8
	v_exp_f32_e32 v6, v6
	v_mul_f32_e32 v7, 0x3fb8aa3b, v7
	v_sub_f32_e32 v8, v58, v4
	v_exp_f32_e32 v7, v7
	v_mul_f32_e32 v8, 0x3fb8aa3b, v8
	v_sub_f32_e32 v9, v59, v4
	v_exp_f32_e32 v8, v8
	v_mul_f32_e32 v9, 0x3fb8aa3b, v9
	v_exp_f32_e32 v9, v9
	v_add_f32_e32 v5, v5, v6
	v_sub_f32_e32 v6, v28, v4
	v_add_f32_e32 v5, v5, v7
	v_mul_f32_e32 v6, 0x3fb8aa3b, v6
	v_sub_f32_e32 v7, v29, v4
	v_add_f32_e32 v5, v5, v8
	v_exp_f32_e32 v6, v6
	v_mul_f32_e32 v7, 0x3fb8aa3b, v7
	v_sub_f32_e32 v8, v30, v4
	v_add_f32_e32 v5, v5, v9
	v_exp_f32_e32 v7, v7
	v_mul_f32_e32 v8, 0x3fb8aa3b, v8
	v_sub_f32_e32 v9, v31, v4
	v_exp_f32_e32 v8, v8
	v_mul_f32_e32 v9, 0x3fb8aa3b, v9
	v_exp_f32_e32 v9, v9
	v_add_f32_e32 v5, v5, v6
	v_sub_f32_e32 v6, v16, v4
	v_add_f32_e32 v5, v5, v7
	v_mul_f32_e32 v6, 0x3fb8aa3b, v6
	v_sub_f32_e32 v7, v17, v4
	v_add_f32_e32 v5, v5, v8
	v_exp_f32_e32 v6, v6
	v_mul_f32_e32 v7, 0x3fb8aa3b, v7
	v_sub_f32_e32 v8, v18, v4
	v_add_f32_e32 v5, v5, v9
	v_exp_f32_e32 v7, v7
	v_mul_f32_e32 v8, 0x3fb8aa3b, v8
	v_sub_f32_e32 v9, v19, v4
	v_exp_f32_e32 v8, v8
	v_mul_f32_e32 v9, 0x3fb8aa3b, v9
	v_exp_f32_e32 v9, v9
	v_add_f32_e32 v5, v5, v6
	v_sub_f32_e32 v6, v0, v4
	v_add_f32_e32 v5, v5, v7
	v_mul_f32_e32 v6, 0x3fb8aa3b, v6
	v_sub_f32_e32 v7, v1, v4
	v_add_f32_e32 v5, v5, v8
	v_exp_f32_e32 v6, v6
	v_mul_f32_e32 v7, 0x3fb8aa3b, v7
	v_sub_f32_e32 v8, v2, v4
	v_add_f32_e32 v5, v5, v9
	v_exp_f32_e32 v7, v7
	v_mul_f32_e32 v8, 0x3fb8aa3b, v8
	v_sub_f32_e32 v9, v3, v4
	v_exp_f32_e32 v8, v8
	v_mul_f32_e32 v9, 0x3fb8aa3b, v9
	v_exp_f32_e32 v9, v9
	v_add_f32_e32 v5, v5, v6
	v_add_f32_e32 v5, v5, v7
	v_add_f32_e32 v5, v5, v8
	v_add_f32_e32 v5, v5, v9
	s_nop 1
	v_mov_b32_dpp v6, v5 quad_perm:[1,0,3,2] row_mask:0xf bank_mask:0xf
	s_and_b64 exec, exec, s[8:9]
	s_cbranch_execz .LBB2_371
	s_waitcnt lgkmcnt(0)
	v_add_f32_e32 v5, v5, v6
	s_mov_b32 s0, 0x800000
	v_cmp_gt_f32_e32 vcc, s0, v5
	s_mov_b32 s0, 0x3f317217
	v_mov_b32_e32 v67, 0
	v_cndmask_b32_e64 v6, 0, 32, vcc
	v_ldexp_f32 v5, v5, v6
	v_log_f32_e32 v5, v5
	s_nop 0
	v_mul_f32_e32 v6, 0x3f317217, v5
	v_fma_f32 v6, v5, s0, -v6
	v_fmamk_f32 v6, v5, 0x3377d1cf, v6
	s_mov_b32 s0, 0x7f800000
	v_fmac_f32_e32 v6, 0x3f317217, v5
	v_cmp_lt_f32_e64 s[0:1], |v5|, s0
	s_nop 1
	v_cndmask_b32_e64 v5, v5, v6, s[0:1]
	v_mov_b32_e32 v6, 0x41b17218
	v_cndmask_b32_e32 v6, 0, v6, vcc
	v_sub_f32_e32 v5, v5, v6
	v_add_f32_e32 v10, v4, v5
	s_movk_i32 s0, 0xa0
	v_mov_b64_e32 v[4:5], s[52:53]
	v_mad_i64_i32 v[4:5], s[0:1], v64, s0, v[4:5]
	v_lshl_add_u64 v[8:9], v[4:5], 0, v[66:67]
	v_sub_f32_e32 v7, v99, v10
	v_sub_f32_e32 v6, v98, v10
	v_sub_f32_e32 v5, v93, v10
	v_sub_f32_e32 v4, v92, v10
	global_store_dwordx4 v[8:9], v[4:7], off
	v_sub_f32_e32 v3, v3, v10
	v_sub_f32_e32 v2, v2, v10
	v_sub_f32_e32 v7, v59, v10
	v_sub_f32_e32 v6, v58, v10
	v_sub_f32_e32 v5, v57, v10
	v_sub_f32_e32 v4, v56, v10
	global_store_dwordx4 v[8:9], v[4:7], off offset:16
	v_sub_f32_e32 v1, v1, v10
	v_sub_f32_e32 v0, v0, v10
	v_sub_f32_e32 v7, v31, v10
	v_sub_f32_e32 v6, v30, v10
	v_sub_f32_e32 v5, v29, v10
	v_sub_f32_e32 v4, v28, v10
	global_store_dwordx4 v[8:9], v[4:7], off offset:32
	global_store_dwordx4 v[8:9], v[0:3], off offset:64
	s_nop 0
	v_sub_f32_e32 v7, v19, v10
	v_sub_f32_e32 v6, v18, v10
	v_sub_f32_e32 v5, v17, v10
	v_sub_f32_e32 v4, v16, v10
	global_store_dwordx4 v[8:9], v[4:7], off offset:48
